# P12: final_norm_w chunks hoisted out of the row loop into v200-231; 8 output stores back-to-back (no vmcnt(0) ladder)
# speedup vs baseline: 1.0206x; 1.0037x over previous
; #define UNP4(v) ((f32x4){__uint_as_float((v).x << 16), __uint_as_float((v).x & 0xffff0000u), __uint_as_float((v).y << 16), __uint_as_float((v).y & 0xffff0000u)})
; __device__ __forceinline__ void p12_final(Frame& F) {
;     const bf16* X1 = (const bf16*)(F.ws + WS_X1); const unsigned char* YS = (const unsigned char*)(F.ws + WS_YS); const float* fw = F.in[I_FNW];
;     const int gw = F.bid * NWAVES + F.wave, NGW = F.G * NWAVES;
;     for (int m = gw; m < T; m += NGW) {
;         const v2u* xr = (const v2u*)(X1 + (size_t)m * D) + F.lane; f32x4 v[8]; float s = 0.f;
; #pragma unroll
;         for (int j = 0; j < 8; ++j) { const v2u xb_ = xr[64 * j]; v[j] = UNP4(xb_);
; #pragma unroll
;             for (int sl = 0; sl < 4; ++sl) { const int y = ((const int*)(YS + ((size_t)m * 4 + sl) * D))[F.lane + 64 * j];
;                 const f32x2 ylo = __builtin_amdgcn_cvt_pk_f32_fp8(y, false), yhi = __builtin_amdgcn_cvt_pk_f32_fp8(y, true);
;                 v[j][0] += ylo[0] * (1.f / F8_SY); v[j][1] += ylo[1] * (1.f / F8_SY); v[j][2] += yhi[0] * (1.f / F8_SY); v[j][3] += yhi[1] * (1.f / F8_SY); }
;             s += (v[j][0] * v[j][0] + v[j][1] * v[j][1]) + (v[j][2] * v[j][2] + v[j][3] * v[j][3]); }
.LBB0_2458:
	s_cmp_lt_i32 s78, 13
	s_cselect_b64 s[2:3], -1, 0
	s_and_b64 s[0:1], s[2:3], s[0:1]
	s_andn2_b64 vcc, exec, s[0:1]
	s_cbranch_vccnz .LBB0_2462
	s_lshl_b32 s0, s74, 3
	s_add_i32 s0, s92, s0
	s_cmpk_gt_i32 s0, 0x3fff
	s_cbranch_scc1 .LBB0_2462
	s_waitcnt vmcnt(0)
	v_mbcnt_lo_u32_b32 v2, -1, 0
	v_mbcnt_hi_u32_b32 v2, -1, v2
	v_and_b32_e32 v3, 64, v2
	v_add_u32_e32 v3, 64, v3
	v_xor_b32_e32 v14, 1, v2
	v_cmp_lt_i32_e32 vcc, v14, v3
	v_lshlrev_b32_e32 v0, 4, v162
	v_mov_b32_e32 v1, 0
	v_cndmask_b32_e32 v14, v2, v14, vcc
	v_lshlrev_b32_e32 v28, 2, v14
	v_xor_b32_e32 v14, 2, v2
	v_cmp_lt_i32_e32 vcc, v14, v3
	v_lshl_add_u64 v[4:5], s[86:87], 0, v[0:1]
	s_mov_b64 s[4:5], 0x1400
	v_cndmask_b32_e32 v14, v2, v14, vcc
	v_lshlrev_b32_e32 v29, 2, v14
	v_xor_b32_e32 v14, 4, v2
	v_cmp_lt_i32_e32 vcc, v14, v3
	s_lshl_b32 s2, s72, 3
	v_lshl_add_u64 v[8:9], v[4:5], 0, s[4:5]
	v_cndmask_b32_e32 v14, v2, v14, vcc
	v_lshlrev_b32_e32 v30, 2, v14
	v_xor_b32_e32 v14, 8, v2
	v_cmp_lt_i32_e32 vcc, v14, v3
	s_mov_b64 s[4:5], 0x1800
	s_ashr_i32 s1, s0, 31
	v_cndmask_b32_e32 v14, v2, v14, vcc
	v_lshlrev_b32_e32 v31, 2, v14
	v_xor_b32_e32 v14, 16, v2
	v_cmp_lt_i32_e32 vcc, v14, v3
	v_lshl_add_u64 v[10:11], v[4:5], 0, s[4:5]
	s_mov_b64 s[4:5], 0x1c00
	v_cndmask_b32_e32 v14, v2, v14, vcc
	v_lshlrev_b32_e32 v32, 2, v14
	v_xor_b32_e32 v14, 32, v2
	s_ashr_i32 s3, s2, 31
	s_lshl_b64 s[6:7], s[0:1], 12
	v_lshl_add_u64 v[12:13], v[4:5], 0, s[4:5]
	v_cmp_lt_i32_e32 vcc, v14, v3
	s_lshl_b64 s[10:11], s[0:1], 13
	s_lshl_b64 s[4:5], s[2:3], 13
	v_lshl_or_b32 v16, v162, 3, s6
	v_mov_b32_e32 v17, s7
	s_lshl_b64 s[6:7], s[2:3], 12
	v_cndmask_b32_e32 v2, v2, v14, vcc
	v_lshl_or_b32 v14, v162, 2, s10
	s_add_u32 s10, s88, s10
	v_mov_b32_e32 v15, s11
	s_addc_u32 s11, s89, s11
	s_mov_b64 s[8:9], 0x1000
	v_lshl_add_u64 v[0:1], s[10:11], 0, v[0:1]
	v_lshl_add_u64 v[6:7], v[4:5], 0, s[8:9]
	v_lshl_add_u64 v[18:19], v[0:1], 0, s[8:9]
	s_mov_b32 s8, 0x3d800000
	v_lshlrev_b32_e32 v33, 2, v2
	s_mov_b32 s1, s8
	v_mov_b32_e32 v34, 0x358637bd
	v_mov_b32_e32 v21, 0x3d800000
	global_load_dwordx4 v[200:203], v[4:5], off
	global_load_dwordx4 v[204:207], v[4:5], off offset:1024
	global_load_dwordx4 v[208:211], v[4:5], off offset:2048
	global_load_dwordx4 v[212:215], v[4:5], off offset:3072
	global_load_dwordx4 v[216:219], v[6:7], off
	global_load_dwordx4 v[220:223], v[8:9], off
	global_load_dwordx4 v[224:227], v[10:11], off
	global_load_dwordx4 v[228:231], v[12:13], off
.LBB0_2461:
	v_lshl_add_u64 v[24:25], s[90:91], 0, v[16:17]
	v_add_co_u32_e32 v24, vcc, 0x72200000, v24
	v_lshl_add_u64 v[22:23], s[90:91], 0, v[14:15]
	s_nop 0
	v_addc_co_u32_e32 v25, vcc, 0, v25, vcc
	v_add_co_u32_e32 v36, vcc, 0x9e200000, v22
	global_load_dwordx2 v[38:39], v[24:25], off
	global_load_dwordx2 v[40:41], v[24:25], off offset:512
	global_load_dwordx2 v[42:43], v[24:25], off offset:1024
	global_load_dwordx2 v[44:45], v[24:25], off offset:1536
	global_load_dwordx2 v[46:47], v[24:25], off offset:2048
	global_load_dwordx2 v[48:49], v[24:25], off offset:2560
	global_load_dwordx2 v[50:51], v[24:25], off offset:3072
	global_load_dwordx2 v[52:53], v[24:25], off offset:3584
	v_addc_co_u32_e32 v37, vcc, 0, v23, vcc
	v_add_co_u32_e32 v22, vcc, 0x9e201000, v22
	global_load_dword v20, v[36:37], off
	global_load_dword v26, v[36:37], off offset:2048
	global_load_dword v35, v[36:37], off offset:256
	global_load_dword v62, v[36:37], off offset:2304
	global_load_dword v80, v[36:37], off offset:512
	global_load_dword v84, v[36:37], off offset:2560
	global_load_dword v88, v[36:37], off offset:768
	global_load_dword v92, v[36:37], off offset:2816
	global_load_dword v96, v[36:37], off offset:1024
	global_load_dword v100, v[36:37], off offset:3072
	global_load_dword v104, v[36:37], off offset:1280
	global_load_dword v108, v[36:37], off offset:3328
	global_load_dword v112, v[36:37], off offset:1536
	global_load_dword v116, v[36:37], off offset:3584
	global_load_dword v120, v[36:37], off offset:1792
	global_load_dword v124, v[36:37], off offset:3840
	v_addc_co_u32_e32 v23, vcc, 0, v23, vcc
	global_load_dword v128, v[22:23], off
	global_load_dword v132, v[22:23], off offset:2048
	global_load_dword v140, v[22:23], off offset:2304
	global_load_dword v136, v[22:23], off offset:256
	global_load_dword v144, v[22:23], off offset:512
	global_load_dword v152, v[22:23], off offset:768
	global_load_dword v160, v[22:23], off offset:1024
	global_load_dword v168, v[22:23], off offset:1280
	global_load_dword v176, v[22:23], off offset:1536
	global_load_dword v184, v[22:23], off offset:1792
	global_load_dword v148, v[22:23], off offset:2560
	global_load_dword v156, v[22:23], off offset:2816
	global_load_dword v164, v[22:23], off offset:3072
	global_load_dword v172, v[22:23], off offset:3328
	global_load_dword v180, v[22:23], off offset:3584
	global_load_dword v188, v[22:23], off offset:3840
	v_mov_b32_e32 v27, v21
	v_lshl_add_u64 v[14:15], v[14:15], 0, s[4:5]
	v_lshl_add_u64 v[16:17], v[16:17], 0, s[6:7]
	s_waitcnt vmcnt(31)
	v_cvt_pk_f32_fp8_sdwa v[64:65], v20 src0_sel:WORD_1
	s_waitcnt vmcnt(30)
	v_cvt_pk_f32_fp8_e32 v[66:67], v26
	s_waitcnt vmcnt(29)
	v_cvt_pk_f32_fp8_e32 v[70:71], v35
	v_cvt_pk_f32_fp8_sdwa v[72:73], v35 src0_sel:WORD_1
	s_waitcnt vmcnt(28)
	v_cvt_pk_f32_fp8_e32 v[74:75], v62
	v_cvt_pk_f32_fp8_sdwa v[76:77], v62 src0_sel:WORD_1
	s_waitcnt vmcnt(27)
	v_cvt_pk_f32_fp8_e32 v[78:79], v80
	v_cvt_pk_f32_fp8_sdwa v[80:81], v80 src0_sel:WORD_1
	s_waitcnt vmcnt(26)
	v_cvt_pk_f32_fp8_e32 v[82:83], v84
	v_cvt_pk_f32_fp8_sdwa v[84:85], v84 src0_sel:WORD_1
	v_lshlrev_b32_e32 v192, 16, v52
	v_and_b32_e32 v63, 0xffff0000, v52
	v_lshlrev_b32_e32 v59, 16, v53
	v_and_b32_e32 v61, 0xffff0000, v53
	v_cvt_pk_f32_fp8_e32 v[52:53], v20
	s_waitcnt vmcnt(25)
; #define UNP4(v) ((f32x4){__uint_as_float((v).x << 16), __uint_as_float((v).x & 0xffff0000u), __uint_as_float((v).y << 16), __uint_as_float((v).y & 0xffff0000u)})
; __device__ __forceinline__ void p12_final(Frame& F) {
;     ...
;         for (int j = 0; j < 8; ++j) { const v2u xb_ = xr[64 * j]; v[j] = UNP4(xb_);
; #pragma unroll
;             for (int sl = 0; sl < 4; ++sl) { const int y = ((const int*)(YS + ((size_t)m * 4 + sl) * D))[F.lane + 64 * j];
;                 const f32x2 ylo = __builtin_amdgcn_cvt_pk_f32_fp8(y, false), yhi = __builtin_amdgcn_cvt_pk_f32_fp8(y, true);
;                 v[j][0] += ylo[0] * (1.f / F8_SY); v[j][1] += ylo[1] * (1.f / F8_SY); v[j][2] += yhi[0] * (1.f / F8_SY); v[j][3] += yhi[1] * (1.f / F8_SY); }
;             s += (v[j][0] * v[j][0] + v[j][1] * v[j][1]) + (v[j][2] * v[j][2] + v[j][3] * v[j][3]); }
	v_cvt_pk_f32_fp8_e32 v[86:87], v88
	v_cvt_pk_f32_fp8_sdwa v[88:89], v88 src0_sel:WORD_1
	s_waitcnt vmcnt(24)
	v_cvt_pk_f32_fp8_e32 v[90:91], v92
	v_cvt_pk_f32_fp8_sdwa v[92:93], v92 src0_sel:WORD_1
	s_waitcnt vmcnt(23)
	v_cvt_pk_f32_fp8_e32 v[94:95], v96
	v_cvt_pk_f32_fp8_sdwa v[96:97], v96 src0_sel:WORD_1
	s_waitcnt vmcnt(22)
	v_cvt_pk_f32_fp8_e32 v[98:99], v100
	s_waitcnt vmcnt(21)
	v_cvt_pk_f32_fp8_e32 v[102:103], v104
	v_cvt_pk_f32_fp8_sdwa v[104:105], v104 src0_sel:WORD_1
	s_waitcnt vmcnt(20)
	v_cvt_pk_f32_fp8_e32 v[106:107], v108
	v_cvt_pk_f32_fp8_sdwa v[108:109], v108 src0_sel:WORD_1
	v_cvt_pk_f32_fp8_sdwa v[68:69], v26 src0_sel:WORD_1
	v_cvt_pk_f32_fp8_sdwa v[100:101], v100 src0_sel:WORD_1
	s_waitcnt vmcnt(15)
	v_cvt_pk_f32_fp8_e32 v[126:127], v128
	v_cvt_pk_f32_fp8_sdwa v[128:129], v128 src0_sel:WORD_1
	s_waitcnt vmcnt(12)
	v_cvt_pk_f32_fp8_e32 v[134:135], v136
	v_cvt_pk_f32_fp8_sdwa v[136:137], v136 src0_sel:WORD_1
	s_waitcnt vmcnt(9)
	v_cvt_pk_f32_fp8_e32 v[158:159], v160
	s_waitcnt vmcnt(3)
	v_cvt_pk_f32_fp8_e32 v[162:163], v164
	v_cvt_pk_f32_fp8_e32 v[166:167], v168
	v_cvt_pk_f32_fp8_sdwa v[168:169], v168 src0_sel:WORD_1
	s_waitcnt vmcnt(2)
	v_cvt_pk_f32_fp8_e32 v[170:171], v172
	v_cvt_pk_f32_fp8_sdwa v[172:173], v172 src0_sel:WORD_1
	v_lshlrev_b32_e32 v22, 16, v38
	v_and_b32_e32 v23, 0xffff0000, v38
	v_lshlrev_b32_e32 v24, 16, v39
	v_and_b32_e32 v25, 0xffff0000, v39
	v_lshlrev_b32_e32 v56, 16, v46
	v_and_b32_e32 v57, 0xffff0000, v46
	v_lshlrev_b32_e32 v46, 16, v47
	v_and_b32_e32 v47, 0xffff0000, v47
	v_cvt_pk_f32_fp8_e32 v[130:131], v132
	v_cvt_pk_f32_fp8_sdwa v[132:133], v132 src0_sel:WORD_1
	v_cvt_pk_f32_fp8_e32 v[138:139], v140
	v_cvt_pk_f32_fp8_sdwa v[140:141], v140 src0_sel:WORD_1
	v_cvt_pk_f32_fp8_e32 v[142:143], v144
	v_cvt_pk_f32_fp8_sdwa v[144:145], v144 src0_sel:WORD_1
	v_cvt_pk_f32_fp8_e32 v[150:151], v152
	v_cvt_pk_f32_fp8_sdwa v[152:153], v152 src0_sel:WORD_1
	v_lshlrev_b32_e32 v37, 16, v41
	v_lshlrev_b32_e32 v36, 16, v40
	v_and_b32_e32 v39, 0xffff0000, v41
	v_and_b32_e32 v38, 0xffff0000, v40
	v_lshlrev_b32_e32 v41, 16, v43
	v_lshlrev_b32_e32 v40, 16, v42
	v_and_b32_e32 v43, 0xffff0000, v43
	v_and_b32_e32 v42, 0xffff0000, v42
	v_cvt_pk_f32_fp8_e32 v[110:111], v112
	v_cvt_pk_f32_fp8_e32 v[114:115], v116
	v_cvt_pk_f32_fp8_e32 v[118:119], v120
	v_cvt_pk_f32_fp8_sdwa v[120:121], v120 src0_sel:WORD_1
	v_cvt_pk_f32_fp8_e32 v[146:147], v148
	v_cvt_pk_f32_fp8_sdwa v[148:149], v148 src0_sel:WORD_1
	v_pk_fma_f32 v[22:23], v[52:53], s[8:9], v[22:23] op_sel_hi:[1,0,1]
	v_pk_fma_f32 v[24:25], v[64:65], s[8:9], v[24:25] op_sel_hi:[1,0,1]
	v_mov_b32_e32 v52, v70
	v_mov_b32_e32 v53, v72
	v_mov_b32_e32 v72, v71
	v_mov_b32_e32 v65, v76
	v_mov_b32_e32 v76, v75
	v_mov_b32_e32 v70, v78
	v_mov_b32_e32 v71, v80
	v_mov_b32_e32 v80, v79
	v_mov_b32_e32 v75, v84
	v_mov_b32_e32 v84, v83
	v_mov_b32_e32 v78, v86
	v_mov_b32_e32 v79, v88
	v_mov_b32_e32 v88, v87
	v_mov_b32_e32 v83, v92
	v_mov_b32_e32 v92, v91
	v_mov_b32_e32 v86, v94
	v_mov_b32_e32 v87, v98
	v_mov_b32_e32 v98, v95
	v_pk_fma_f32 v[46:47], v[96:97], s[8:9], v[46:47] op_sel_hi:[1,0,1]
	v_mov_b32_e32 v91, v106
	v_mov_b32_e32 v106, v103
	v_mov_b32_e32 v94, v104
	v_mov_b32_e32 v95, v108
	v_mov_b32_e32 v108, v105
	v_lshlrev_b32_e32 v55, 16, v45
	v_lshlrev_b32_e32 v54, 16, v44
	v_and_b32_e32 v45, 0xffff0000, v45
	v_and_b32_e32 v44, 0xffff0000, v44
	v_and_b32_e32 v191, 0xffff0000, v49
	v_cvt_pk_f32_fp8_sdwa v[112:113], v112 src0_sel:WORD_1
	v_cvt_pk_f32_fp8_sdwa v[116:117], v116 src0_sel:WORD_1
	v_mov_b32_e32 v64, v74
	v_pk_fma_f32 v[22:23], v[66:67], s[8:9], v[22:23] op_sel_hi:[1,0,1]
	v_pk_fma_f32 v[24:25], v[68:69], s[8:9], v[24:25] op_sel_hi:[1,0,1]
	v_pk_fma_f32 v[36:37], v[52:53], s[8:9], v[36:37] op_sel_hi:[1,0,1]
	v_pk_fma_f32 v[38:39], v[72:73], s[8:9], v[38:39] op_sel_hi:[1,0,1]
	v_pk_fma_f32 v[42:43], v[80:81], s[8:9], v[42:43] op_sel_hi:[1,0,1]
	v_pk_mul_f32 v[80:81], v[86:87], s[8:9] op_sel_hi:[1,0]
	v_pk_mul_f32 v[86:87], v[98:99], s[8:9] op_sel_hi:[1,0]
	v_pk_fma_f32 v[46:47], v[100:101], s[8:9], v[46:47] op_sel_hi:[1,0,1]
	v_pk_mul_f32 v[98:99], v[106:107], s[8:9] op_sel_hi:[1,0]
	v_pk_mul_f32 v[94:95], v[94:95], s[8:9] op_sel_hi:[1,0]
	v_pk_mul_f32 v[100:101], v[108:109], s[8:9] op_sel_hi:[1,0]
	v_lshlrev_b32_e32 v190, 16, v48
	v_and_b32_e32 v48, 0xffff0000, v48
	v_lshlrev_b32_e32 v49, 16, v49
	v_cvt_pk_f32_fp8_e32 v[154:155], v156
	v_cvt_pk_f32_fp8_sdwa v[156:157], v156 src0_sel:WORD_1
	v_cvt_pk_f32_fp8_sdwa v[160:161], v160 src0_sel:WORD_1
	v_mov_b32_e32 v74, v82
	v_mov_b32_e32 v82, v90
	v_mov_b32_e32 v52, v134
	v_mov_b32_e32 v53, v136
	v_mov_b32_e32 v136, v135
	v_pk_fma_f32 v[40:41], v[70:71], s[8:9], v[40:41] op_sel_hi:[1,0,1]
	v_pk_fma_f32 v[54:55], v[78:79], s[8:9], v[54:55] op_sel_hi:[1,0,1]
	v_pk_fma_f32 v[44:45], v[88:89], s[8:9], v[44:45] op_sel_hi:[1,0,1]
	v_mov_b32_e32 v88, v158
	v_mov_b32_e32 v89, v162
	v_mov_b32_e32 v162, v159
	v_mov_b32_e32 v104, v167
	v_mov_b32_e32 v105, v171
	v_mov_b32_e32 v106, v168
	v_mov_b32_e32 v107, v172
	v_mov_b32_e32 v172, v169
	v_pk_fma_f32 v[22:23], v[126:127], s[8:9], v[22:23] op_sel_hi:[1,0,1]
	v_pk_fma_f32 v[24:25], v[128:129], s[8:9], v[24:25] op_sel_hi:[1,0,1]
	v_pk_fma_f32 v[36:37], v[64:65], s[8:9], v[36:37] op_sel_hi:[1,0,1]
	v_pk_fma_f32 v[38:39], v[76:77], s[8:9], v[38:39] op_sel_hi:[1,0,1]
	v_pk_fma_f32 v[42:43], v[84:85], s[8:9], v[42:43] op_sel_hi:[1,0,1]
	v_add_f32_e32 v26, v100, v191
	v_mov_b32_e32 v84, v98
	v_mov_b32_e32 v85, v94
	v_lshlrev_b32_e32 v58, 16, v50
	v_cvt_pk_f32_fp8_e32 v[122:123], v124
	v_cvt_pk_f32_fp8_sdwa v[164:165], v164 src0_sel:WORD_1
	v_cvt_pk_f32_fp8_e32 v[174:175], v176
	v_cvt_pk_f32_fp8_sdwa v[176:177], v176 src0_sel:WORD_1
	s_waitcnt vmcnt(1)
; #define UNP4(v) ((f32x4){__uint_as_float((v).x << 16), __uint_as_float((v).x & 0xffff0000u), __uint_as_float((v).y << 16), __uint_as_float((v).y & 0xffff0000u)})
; __device__ __forceinline__ void p12_final(Frame& F) {
;     ...
;         for (int j = 0; j < 8; ++j) { const v2u xb_ = xr[64 * j]; v[j] = UNP4(xb_);
; #pragma unroll
;             for (int sl = 0; sl < 4; ++sl) { const int y = ((const int*)(YS + ((size_t)m * 4 + sl) * D))[F.lane + 64 * j];
;                 const f32x2 ylo = __builtin_amdgcn_cvt_pk_f32_fp8(y, false), yhi = __builtin_amdgcn_cvt_pk_f32_fp8(y, true);
;                 v[j][0] += ylo[0] * (1.f / F8_SY); v[j][1] += ylo[1] * (1.f / F8_SY); v[j][2] += yhi[0] * (1.f / F8_SY); v[j][3] += yhi[1] * (1.f / F8_SY); }
;             s += (v[j][0] * v[j][0] + v[j][1] * v[j][1]) + (v[j][2] * v[j][2] + v[j][3] * v[j][3]); }
	v_cvt_pk_f32_fp8_e32 v[178:179], v180
	v_cvt_pk_f32_fp8_sdwa v[180:181], v180 src0_sel:WORD_1
	v_mov_b32_e32 v90, v102
	v_mov_b32_e32 v66, v138
	v_mov_b32_e32 v67, v140
	v_mov_b32_e32 v140, v139
	v_mov_b32_e32 v68, v142
	v_mov_b32_e32 v69, v144
	v_mov_b32_e32 v72, v150
	v_mov_b32_e32 v73, v152
	v_pk_fma_f32 v[40:41], v[74:75], s[8:9], v[40:41] op_sel_hi:[1,0,1]
	v_pk_fma_f32 v[54:55], v[82:83], s[8:9], v[54:55] op_sel_hi:[1,0,1]
	v_pk_mul_f32 v[64:65], v[88:89], s[8:9] op_sel_hi:[1,0]
	v_pk_mul_f32 v[74:75], v[162:163], s[8:9] op_sel_hi:[1,0]
	v_mov_b32_e32 v76, v80
	v_mov_b32_e32 v77, v86
	v_mov_b32_e32 v86, v81
	v_pk_mul_f32 v[80:81], v[104:105], s[8:9] op_sel_hi:[1,0]
	v_pk_mul_f32 v[82:83], v[106:107], s[8:9] op_sel_hi:[1,0]
	v_mov_b32_e32 v94, v99
	v_pk_mul_f32 v[88:89], v[172:173], s[8:9] op_sel_hi:[1,0]
	v_pk_fma_f32 v[22:23], v[130:131], s[8:9], v[22:23] op_sel_hi:[1,0,1]
	v_pk_fma_f32 v[24:25], v[132:133], s[8:9], v[24:25] op_sel_hi:[1,0,1]
	v_pk_fma_f32 v[36:37], v[52:53], s[8:9], v[36:37] op_sel_hi:[1,0,1]
	v_pk_fma_f32 v[38:39], v[136:137], s[8:9], v[38:39] op_sel_hi:[1,0,1]
	v_add_f32_e32 v26, v26, v101
	v_pk_add_f32 v[48:49], v[84:85], v[48:49]
	v_cvt_pk_f32_fp8_sdwa v[124:125], v124 src0_sel:WORD_1
	v_cvt_pk_f32_fp8_e32 v[182:183], v184
	v_fmac_f32_e32 v58, 0x3d800000, v110
	v_mov_b32_e32 v97, v115
	v_mov_b32_e32 v115, v120
	v_mov_b32_e32 v144, v143
	v_mov_b32_e32 v70, v146
	v_mov_b32_e32 v71, v148
	v_pk_mul_f32 v[90:91], v[90:91], s[8:9] op_sel_hi:[1,0]
	v_pk_fma_f32 v[40:41], v[68:69], s[8:9], v[40:41] op_sel_hi:[1,0,1]
	v_pk_fma_f32 v[52:53], v[72:73], s[8:9], v[54:55] op_sel_hi:[1,0,1]
	v_pk_add_f32 v[54:55], v[76:77], v[56:57]
	v_mov_b32_e32 v56, v64
	v_mov_b32_e32 v57, v74
	v_mov_b32_e32 v74, v65
	v_mov_b32_e32 v64, v80
	v_mov_b32_e32 v65, v82
	v_pk_fma_f32 v[36:37], v[66:67], s[8:9], v[36:37] op_sel_hi:[1,0,1]
	v_pk_fma_f32 v[38:39], v[140:141], s[8:9], v[38:39] op_sel_hi:[1,0,1]
	v_pk_add_f32 v[48:49], v[48:49], v[94:95]
	v_add_f32_e32 v67, v26, v88
	v_mul_f32_e32 v26, v23, v23
	v_mul_f32_e32 v66, v25, v25
	v_cvt_pk_f32_fp8_sdwa v[184:185], v184 src0_sel:WORD_1
	v_mov_b32_e32 v96, v111
	v_mov_b32_e32 v102, v113
	v_mov_b32_e32 v103, v117
	v_mul_f32_e32 v35, 0x3d800000, v118
	v_mov_b32_e32 v148, v147
	v_mov_b32_e32 v152, v151
	v_pk_fma_f32 v[58:59], v[114:115], s[8:9], v[58:59] op_sel_hi:[1,0,1]
	v_pk_fma_f32 v[44:45], v[92:93], s[8:9], v[44:45] op_sel_hi:[1,0,1]
	v_add_f32_e32 v20, v90, v190
	v_pk_fma_f32 v[42:43], v[144:145], s[8:9], v[42:43] op_sel_hi:[1,0,1]
	v_pk_fma_f32 v[40:41], v[70:71], s[8:9], v[40:41] op_sel_hi:[1,0,1]
	v_pk_add_f32 v[54:55], v[54:55], v[86:87]
	v_pk_mul_f32 v[70:71], v[38:39], v[38:39]
	v_pk_add_f32 v[48:49], v[48:49], v[64:65]
	v_add_f32_e32 v114, v67, v89
	v_pk_fma_f32 v[64:65], v[22:23], v[22:23], v[26:27] op_sel_hi:[1,1,0]
	v_pk_fma_f32 v[66:67], v[24:25], v[24:25], v[66:67] op_sel_hi:[1,1,0]
	v_lshlrev_b32_e32 v60, 16, v51
	s_waitcnt vmcnt(0)
	v_cvt_pk_f32_fp8_e32 v[186:187], v188
	v_mov_b32_e32 v79, v156
	v_mov_b32_e32 v156, v155
	v_pk_mul_f32 v[96:97], v[96:97], s[8:9] op_sel_hi:[1,0]
	v_pk_mul_f32 v[102:103], v[102:103], s[8:9] op_sel_hi:[1,0]
	v_mov_b32_e32 v167, v119
	v_pk_fma_f32 v[46:47], v[160:161], s[8:9], v[46:47] op_sel_hi:[1,0,1]
	v_pk_fma_f32 v[44:45], v[152:153], s[8:9], v[44:45] op_sel_hi:[1,0,1]
	v_add_f32_e32 v62, v20, v91
	v_pk_fma_f32 v[42:43], v[148:149], s[8:9], v[42:43] op_sel_hi:[1,0,1]
	v_pk_add_f32 v[54:55], v[54:55], v[56:57]
	v_pk_fma_f32 v[70:71], v[36:37], v[36:37], v[70:71]
	v_mov_b32_e32 v65, v35
	v_mov_b32_e32 v67, v192
	v_and_b32_e32 v51, 0xffff0000, v51
	v_and_b32_e32 v50, 0xffff0000, v50
	v_cvt_pk_f32_fp8_sdwa v[188:189], v188 src0_sel:WORD_1
	v_fmac_f32_e32 v60, 0x3d800000, v112
	v_mul_f32_e32 v118, 0x3d800000, v122
	v_mov_b32_e32 v117, v121
	v_mov_b32_e32 v78, v154
	v_mov_b32_e32 v108, v175
	v_mov_b32_e32 v109, v179
	v_mov_b32_e32 v110, v177
	v_mov_b32_e32 v111, v181
	v_mov_b32_e32 v171, v123
	v_mov_b32_e32 v104, v96
	v_mov_b32_e32 v105, v102
	v_pk_fma_f32 v[46:47], v[164:165], s[8:9], v[46:47] op_sel_hi:[1,0,1]
	v_pk_fma_f32 v[44:45], v[156:157], s[8:9], v[44:45] op_sel_hi:[1,0,1]
	v_pk_fma_f32 v[62:63], v[166:167], s[8:9], v[62:63] op_sel_hi:[1,0,1]
	v_pk_mul_f32 v[72:73], v[42:43], v[42:43]
	v_pk_add_f32 v[54:55], v[54:55], v[74:75]
	v_pk_add_f32 v[64:65], v[64:65], v[66:67]
	v_pk_add_f32 v[66:67], v[70:71], v[70:71] op_sel:[0,1] op_sel_hi:[1,0]
	v_pk_fma_f32 v[60:61], v[116:117], s[8:9], v[60:61] op_sel_hi:[1,0,1]
	v_mov_b32_e32 v175, v124
	v_mov_b32_e32 v177, v125
	v_pk_mul_f32 v[92:93], v[108:109], s[8:9] op_sel_hi:[1,0]
	v_pk_mul_f32 v[98:99], v[110:111], s[8:9] op_sel_hi:[1,0]
	v_mov_b32_e32 v102, v97
	v_mov_b32_e32 v82, v81
	v_pk_add_f32 v[50:51], v[104:105], v[50:51]
	v_pk_fma_f32 v[52:53], v[78:79], s[8:9], v[52:53] op_sel_hi:[1,0,1]
	v_mul_f32_e32 v20, v47, v47
	v_pk_mul_f32 v[76:77], v[44:45], v[44:45]
	v_pk_fma_f32 v[62:63], v[170:171], s[8:9], v[62:63] op_sel_hi:[1,0,1]
	v_pk_fma_f32 v[72:73], v[40:41], v[40:41], v[72:73]
	v_pk_mov_b32 v[70:71], v[54:55], v[182:183] op_sel:[1,0]
	v_mov_b32_e32 v67, v118
	v_mul_f32_e32 v113, 0x3d800000, v183
	v_mov_b32_e32 v179, v184
	v_mov_b32_e32 v181, v185
	v_pk_fma_f32 v[58:59], v[174:175], s[8:9], v[58:59] op_sel_hi:[1,0,1]
	v_pk_fma_f32 v[60:61], v[176:177], s[8:9], v[60:61] op_sel_hi:[1,0,1]
	v_mov_b32_e32 v68, v92
	v_mov_b32_e32 v69, v98
	v_mov_b32_e32 v98, v93
	v_pk_add_f32 v[50:51], v[50:51], v[102:103]
; __device__ __forceinline__ float wave_sum(float v) {
; #pragma unroll
;     for (int o = 1; o < 64; o <<= 1) v += __shfl_xor(v, o);
;     return v;
; }
; __device__ __forceinline__ void p12_final(Frame& F) {
;     ...
;             s += (v[j][0] * v[j][0] + v[j][1] * v[j][1]) + (v[j][2] * v[j][2] + v[j][3] * v[j][3]); }
;         const float rstd = __builtin_amdgcn_rsqf(wave_sum(s) * (1.f / D) + NORM_EPS);
;         f32x4* orow = (f32x4*)(F.out + (size_t)m * D) + F.lane;
; #pragma unroll
;         for (int j = 0; j < 8; ++j) { const f32x4 w = ((const f32x4*)fw)[F.lane + 64 * j]; orow[64 * j] = v[j] * rstd * w; }
	v_pk_fma_f32 v[56:57], v[46:47], v[46:47], v[20:21] op_sel_hi:[1,1,0]
	v_pk_fma_f32 v[76:77], v[52:53], v[52:53], v[76:77]
	v_pk_add_f32 v[48:49], v[48:49], v[82:83]
	v_mov_b32_e32 v112, v62
	v_pk_add_f32 v[72:73], v[72:73], v[72:73] op_sel:[0,1] op_sel_hi:[1,0]
	v_pk_mul_f32 v[84:85], v[54:55], v[54:55]
	v_pk_mul_f32 v[92:93], v[70:71], s[0:1]
	v_pk_add_f32 v[64:65], v[64:65], v[66:67]
	v_pk_fma_f32 v[58:59], v[178:179], s[8:9], v[58:59] op_sel_hi:[1,0,1]
	v_pk_fma_f32 v[60:61], v[180:181], s[8:9], v[60:61] op_sel_hi:[1,0,1]
	v_pk_add_f32 v[50:51], v[50:51], v[68:69]
	v_mul_f32_e32 v57, 0x3d800000, v186
	v_pk_mul_f32 v[74:75], v[62:63], v[62:63]
	v_pk_mul_f32 v[86:87], v[48:49], v[48:49]
	v_mov_b32_e32 v20, v55
	v_pk_add_f32 v[90:91], v[62:63], v[112:113]
	v_pk_add_f32 v[76:77], v[76:77], v[76:77] op_sel:[0,1] op_sel_hi:[1,0]
	v_mov_b32_e32 v73, v93
	v_mov_b32_e32 v85, v65
	v_mul_f32_e32 v121, 0x3d800000, v188
	v_mul_f32_e32 v135, 0x3d800000, v189
	v_mov_b32_e32 v115, v187
	v_mov_b32_e32 v120, v58
	v_mov_b32_e32 v134, v60
	v_pk_add_f32 v[50:51], v[50:51], v[98:99]
	v_mov_b32_e32 v26, v114
	v_mov_b32_e32 v186, v48
	v_mov_b32_e32 v75, v91
	v_mov_b32_e32 v77, v57
	v_mov_b32_e32 v90, v87
	v_pk_add_f32 v[66:67], v[64:65], v[72:73]
	v_pk_fma_f32 v[70:71], v[70:71], v[20:21], v[84:85]
	v_mov_b32_e32 v20, v48
	v_pk_add_f32 v[68:69], v[58:59], v[120:121]
	v_pk_add_f32 v[78:79], v[60:61], v[134:135]
	v_pk_mul_f32 v[88:89], v[50:51], v[50:51]
	v_pk_fma_f32 v[26:27], v[114:115], v[26:27], v[90:91]
	v_pk_add_f32 v[66:67], v[66:67], v[76:77]
	v_pk_add_f32 v[56:57], v[70:71], v[56:57]
	v_pk_fma_f32 v[70:71], v[186:187], v[20:21], v[74:75]
	v_pk_mul_f32 v[80:81], v[68:69], v[68:69]
	v_pk_mul_f32 v[82:83], v[78:79], v[78:79]
	v_pk_fma_f32 v[86:87], v[58:59], v[58:59], v[88:89]
	v_pk_fma_f32 v[88:89], v[60:61], v[60:61], v[88:89] op_sel:[0,0,1] op_sel_hi:[1,1,0]
	v_pk_add_f32 v[72:73], v[66:67], v[56:57]
	v_pk_mul_f32 v[56:57], v[66:67], v[56:57]
	v_pk_add_f32 v[74:75], v[70:71], v[26:27]
	v_pk_mul_f32 v[26:27], v[70:71], v[26:27]
	v_mov_b32_e32 v87, v81
	v_mov_b32_e32 v89, v83
	v_mov_b32_e32 v73, v57
	v_mov_b32_e32 v75, v27
	v_pk_add_f32 v[64:65], v[86:87], v[88:89]
	v_pk_add_f32 v[26:27], v[72:73], v[74:75]
	v_mov_b32_e32 v63, v48
	v_pk_add_f32 v[26:27], v[26:27], v[64:65]
	v_mov_b32_e32 v61, v51
	v_add_f32_e32 v20, v26, v27
	ds_bpermute_b32 v26, v28, v20
	v_mov_b32_e32 v59, v50
	v_mov_b32_e32 v78, v69
	v_mov_b32_e32 v70, v67
	s_add_i32 s0, s0, s2
	s_waitcnt lgkmcnt(0)
	v_add_f32_e32 v20, v20, v26
	ds_bpermute_b32 v26, v29, v20
	s_cmpk_lt_i32 s0, 0x4000
	s_waitcnt lgkmcnt(0)
	v_add_f32_e32 v20, v20, v26
	ds_bpermute_b32 v26, v30, v20
	s_waitcnt lgkmcnt(0)
	v_add_f32_e32 v20, v20, v26
	ds_bpermute_b32 v26, v31, v20
	s_waitcnt lgkmcnt(0)
	v_add_f32_e32 v20, v20, v26
	ds_bpermute_b32 v26, v32, v20
	s_waitcnt lgkmcnt(0)
	v_add_f32_e32 v20, v20, v26
	ds_bpermute_b32 v26, v33, v20
	s_waitcnt lgkmcnt(0)
	v_add_f32_e32 v20, v20, v26
	v_fmamk_f32 v20, v20, 0x3a000000, v34
	v_rsq_f32_e32 v20, v20
	s_nop 0
	v_pk_mul_f32 v[22:23], v[22:23], v[20:21] op_sel_hi:[1,0]
	v_pk_mul_f32 v[24:25], v[24:25], v[20:21] op_sel_hi:[1,0]
	v_pk_mul_f32 v[0:1], v[200:201], v[22:23]
	v_pk_mul_f32 v[2:3], v[202:203], v[24:25]
	global_store_dwordx4 v[18:19], v[0:3], off offset:-4096
	v_mov_b32_e32 v22, v37
	v_mov_b32_e32 v23, v39
	v_mov_b32_e32 v37, v38
	v_pk_mul_f32 v[22:23], v[22:23], v[20:21] op_sel_hi:[1,0]
	v_pk_mul_f32 v[24:25], v[36:37], v[20:21] op_sel_hi:[1,0]
	v_pk_mul_f32 v[234:235], v[206:207], v[22:23]
	v_pk_mul_f32 v[232:233], v[204:205], v[24:25]
	global_store_dwordx4 v[18:19], v[232:235], off offset:-3072
	v_mov_b32_e32 v22, v41
	v_mov_b32_e32 v23, v43
	v_mov_b32_e32 v41, v42
	v_pk_mul_f32 v[22:23], v[22:23], v[20:21] op_sel_hi:[1,0]
	v_pk_mul_f32 v[24:25], v[40:41], v[20:21] op_sel_hi:[1,0]
	v_pk_mul_f32 v[2:3], v[210:211], v[22:23]
	v_pk_mul_f32 v[0:1], v[208:209], v[24:25]
	global_store_dwordx4 v[18:19], v[0:3], off offset:-2048
	v_mov_b32_e32 v22, v53
	v_mov_b32_e32 v23, v45
	v_mov_b32_e32 v53, v44
	v_pk_mul_f32 v[22:23], v[22:23], v[20:21] op_sel_hi:[1,0]
	v_pk_mul_f32 v[24:25], v[52:53], v[20:21] op_sel_hi:[1,0]
	v_pk_mul_f32 v[234:235], v[214:215], v[22:23]
	v_pk_mul_f32 v[232:233], v[212:213], v[24:25]
	global_store_dwordx4 v[18:19], v[232:235], off offset:-1024
	v_pk_mul_f32 v[22:23], v[46:47], v[20:21] op_sel_hi:[1,0]
	v_pk_mul_f32 v[24:25], v[54:55], v[20:21] op_sel_hi:[1,0]
	v_pk_mul_f32 v[2:3], v[218:219], v[22:23]
	v_pk_mul_f32 v[0:1], v[216:217], v[24:25]
	global_store_dwordx4 v[18:19], v[0:3], off
	v_mov_b32_e32 v23, v114
	v_mov_b32_e32 v22, v49
	v_pk_mul_f32 v[22:23], v[22:23], v[20:21] op_sel_hi:[1,0]
	v_pk_mul_f32 v[24:25], v[62:63], v[20:21] op_sel_hi:[1,0]
	v_pk_mul_f32 v[234:235], v[222:223], v[22:23]
	v_pk_mul_f32 v[232:233], v[220:221], v[24:25]
	global_store_dwordx4 v[18:19], v[232:235], off offset:1024
	v_pk_mul_f32 v[22:23], v[60:61], v[20:21] op_sel_hi:[1,0]
	v_pk_mul_f32 v[24:25], v[58:59], v[20:21] op_sel_hi:[1,0]
	v_pk_mul_f32 v[2:3], v[22:23], v[226:227]
	v_pk_mul_f32 v[0:1], v[24:25], v[224:225]
	global_store_dwordx4 v[18:19], v[0:3], off offset:2048
	v_pk_mul_f32 v[22:23], v[78:79], v[20:21] op_sel_hi:[1,0]
	v_pk_mul_f32 v[24:25], v[70:71], v[20:21] op_sel_hi:[1,0]
	v_pk_mul_f32 v[234:235], v[22:23], v[230:231]
	v_pk_mul_f32 v[232:233], v[24:25], v[228:229]
	global_store_dwordx4 v[18:19], v[232:235], off offset:3072
	v_lshl_add_u64 v[18:19], v[18:19], 0, s[4:5]
	s_cbranch_scc1 .LBB0_2461
